# s16p + combined stack of the individually validated scheduling edits: L1 gate-dot reads 8 ahead, permlane16/32_swap cross-row reductions, static prio for waves 4-7 in attention, attention back-edge ro
# speedup vs baseline: 1.0129x; 1.0082x over previous
.LBB0_1115:
	s_cmp_lt_u32 s3, 0x40001
	s_mov_b64 s[18:19], 0
	s_cselect_b64 s[20:21], -1, 0
	s_mov_b64 s[22:23], -1
	s_and_b64 vcc, exec, s[20:21]
	s_cbranch_vccnz .LBB0_1112
	s_branch .LBB0_1109
	s_nop 0
	s_nop 0
	s_nop 0
	s_nop 0
	s_nop 0
	s_nop 0
	s_nop 0
	s_nop 0
	s_nop 0
	s_nop 0
	s_nop 0
	s_nop 0
	s_nop 0
	s_nop 0
	s_nop 0
	s_nop 0
	s_nop 0
	s_nop 0
	s_nop 0
	s_nop 0
	s_nop 0
	s_nop 0
	s_nop 0
	s_nop 0
	s_nop 0
	s_nop 0
	s_nop 0
	s_nop 0
	s_nop 0
	s_nop 0
	s_nop 0
	s_nop 0
	s_nop 0
	s_nop 0
	s_nop 0
	s_nop 0
	s_nop 0
	s_nop 0
	s_nop 0
	s_nop 0
	s_nop 0
	s_nop 0
	s_nop 0
	s_nop 0
	s_nop 0
	s_nop 0
	s_nop 0
	s_nop 0
	s_nop 0
	s_nop 0
	s_nop 0
	s_nop 0
	s_nop 0
	s_nop 0
	s_nop 0
	s_nop 0
	s_nop 0
	s_nop 0

; DI unsigned pk2(float lo, float hi) { const f32x2 v = {lo, hi}; return __builtin_bit_cast(unsigned, __builtin_convertvector(v, bf16x2_t)); }
; DI float wave_sum(float v) { v += shx<1>(v); v += shx<2>(v); v += shx<4>(v); v += shx<8>(v); v += shx<16>(v); v += shx<32>(v); return v; }
; template <int MODE, bool SB  > DI void norm_phase(const Params& P, const Frame& F, int L, const void* src_, const float* gain, bool combine) {
;     ...
; #pragma unroll
;         for (int j = 0; j < 8; ++j) { if constexpr (SB) v[j] = (f32x4){bflo(vb[j].x), bfhi(vb[j].x), bflo(vb[j].y), bfhi(vb[j].y)}; else v[j] = vn[j]; }
;         { const int rnx = (row + NWAVES < r_hi) ? row + NWAVES : row;
; #pragma unroll
;           for (int j = 0; j < 8; ++j) { if constexpr (SB) vb[j] = *(const u32x2*)(srcb + (size_t)rnx * D + 4 * F.lane + 256 * j); else vn[j] = *(const f32x4*)(src + (size_t)rnx * D + 4 * F.lane + 256 * j); } }
;         if (MODE == 3 && combine) {
;             const int* SLOT = (const int*)(ws + WS_SLOT); const float* TOPW = (const float*)(ws + WS_TOPW); const bf16* Y = (const bf16*)(ws + WS_T + T_YPERM);
;             const int s1 = SLOT[row * 2], s2 = SLOT[row * 2 + 1]; const float w1 = TOPW[row * 2], w2 = TOPW[row * 2 + 1];
;             u32x2 ya[8], yb[8];
; #pragma unroll
;             for (int j = 0; j < 8; ++j) { ya[j] = *(const u32x2*)(Y + (size_t)s1 * D + 4 * F.lane + 256 * j); yb[j] = *(const u32x2*)(Y + (size_t)s2 * D + 4 * F.lane + 256 * j); }
; #pragma unroll
;             for (int j = 0; j < 8; ++j) { const f32x4 y1 = (f32x4){bflo(ya[j].x), bfhi(ya[j].x), bflo(ya[j].y), bfhi(ya[j].y)}, y2 = (f32x4){bflo(yb[j].x), bfhi(yb[j].x), bflo(yb[j].y), bfhi(yb[j].y)};
;                 v[j] = v[j] + w1 * y1 + w2 * y2;
;                 const u32x2 hb = {pk2(v[j][0], v[j][1]), pk2(v[j][2], v[j][3])}; *(u32x2*)(const_cast<bf16*>(srcb) + (size_t)row * D + 4 * F.lane + 256 * j) = hb;
;                 v[j] = (f32x4){bflo(hb.x), bfhi(hb.x), bflo(hb.y), bfhi(hb.y)}; }
;         }
;         float ss = 0.f;
; #pragma unroll
;         for (int j = 0; j < 8; ++j) ss += (v[j][0] * v[j][0] + v[j][1] * v[j][1]) + (v[j][2] * v[j][2] + v[j][3] * v[j][3]);
;         const float rstd = 1.0f / sqrtf(wave_sum(ss) * (1.0f / D) + EPS);
.LBB0_1648:
	s_waitcnt vmcnt(0)
	v_and_b32_e32 v75, 0xffff0000, v50
	v_and_b32_e32 v77, 0xffff0000, v51
	v_lshlrev_b32_e32 v65, 16, v48
	v_and_b32_e32 v69, 0xffff0000, v48
	v_lshlrev_b32_e32 v74, 16, v50
	v_lshlrev_b32_e32 v76, 16, v51
	v_mul_f32_e32 v48, v77, v77
	v_lshlrev_b32_e32 v78, 16, v52
	v_and_b32_e32 v81, 0xffff0000, v53
	v_and_b32_e32 v80, 0xffff0000, v52
	v_mul_f32_e32 v52, v75, v75
	v_lshlrev_b32_e32 v72, 16, v49
	v_and_b32_e32 v73, 0xffff0000, v49
	v_pk_fma_f32 v[48:49], v[76:77], v[76:77], v[48:49] op_sel_hi:[1,1,0]
	v_lshlrev_b32_e32 v79, 16, v53
	v_pk_mul_f32 v[50:51], v[80:81], v[80:81]
	v_pk_fma_f32 v[52:53], v[74:75], v[74:75], v[52:53] op_sel_hi:[1,1,0]
	v_pk_fma_f32 v[50:51], v[78:79], v[78:79], v[50:51]
	v_lshlrev_b32_e32 v82, 16, v54
	v_and_b32_e32 v83, 0xffff0000, v54
	v_lshlrev_b32_e32 v84, 16, v55
	v_and_b32_e32 v85, 0xffff0000, v55
	v_mov_b32_e32 v64, v52
	v_mov_b32_e32 v54, v48
	v_mov_b32_e32 v55, v65
	v_mul_f32_e32 v47, v69, v69
	v_pk_add_f32 v[48:49], v[52:53], v[48:49]
	v_pk_mul_f32 v[52:53], v[64:65], v[54:55]
	v_pk_add_f32 v[50:51], v[50:51], v[50:51] op_sel:[0,1] op_sel_hi:[1,0]
	v_mov_b32_e32 v49, v53
	v_mov_b32_e32 v51, v47
	v_pk_add_f32 v[48:49], v[48:49], v[50:51]
	v_mul_f32_e32 v50, v83, v83
	v_mul_f32_e32 v52, v85, v85
	v_lshlrev_b32_e32 v97, 16, v56
	v_and_b32_e32 v71, 0xffff0000, v56
	v_lshlrev_b32_e32 v66, 16, v57
	v_and_b32_e32 v67, 0xffff0000, v57
	v_mul_f32_e32 v56, v72, v72
	v_mul_f32_e32 v57, v73, v73
	v_pk_fma_f32 v[50:51], v[82:83], v[82:83], v[50:51] op_sel_hi:[1,1,0]
	v_pk_fma_f32 v[52:53], v[84:85], v[84:85], v[52:53] op_sel_hi:[1,1,0]
	v_mov_b32_e32 v51, v56
	v_mov_b32_e32 v53, v57
	v_pk_add_f32 v[50:51], v[50:51], v[52:53]
	v_and_b32_e32 v173, 0xffff0000, v59
	v_and_b32_e32 v172, 0xffff0000, v58
	v_pk_add_f32 v[48:49], v[48:49], v[50:51]
	v_lshlrev_b32_e32 v171, 16, v59
	v_lshlrev_b32_e32 v170, 16, v58
	v_pk_mul_f32 v[50:51], v[172:173], v[172:173]
	v_and_b32_e32 v177, 0xffff0000, v61
	v_pk_fma_f32 v[50:51], v[170:171], v[170:171], v[50:51]
	v_and_b32_e32 v176, 0xffff0000, v60
	v_pk_add_f32 v[50:51], v[50:51], v[50:51] op_sel:[0,1] op_sel_hi:[1,0]
	v_pk_add_f32 v[48:49], v[48:49], v[48:49] op_sel:[0,1] op_sel_hi:[1,0]
	v_lshlrev_b32_e32 v175, 16, v61
	v_lshlrev_b32_e32 v174, 16, v60
	v_pk_mul_f32 v[52:53], v[176:177], v[176:177]
	v_mov_b32_e32 v96, v48
	v_mov_b32_e32 v54, v50
	v_mov_b32_e32 v55, v97
	v_pk_fma_f32 v[52:53], v[174:175], v[174:175], v[52:53]
	v_pk_add_f32 v[48:49], v[48:49], v[50:51]
	v_pk_mul_f32 v[50:51], v[96:97], v[54:55]
	v_mul_f32_e32 v47, v71, v71
	v_mov_b32_e32 v49, v51
	v_pk_add_f32 v[50:51], v[52:53], v[52:53] op_sel:[0,1] op_sel_hi:[1,0]
	v_and_b32_e32 v179, 0xffff0000, v62
	v_and_b32_e32 v181, 0xffff0000, v63
	v_mov_b32_e32 v51, v47
	v_lshlrev_b32_e32 v178, 16, v62
	v_lshlrev_b32_e32 v180, 16, v63
	v_pk_add_f32 v[48:49], v[48:49], v[50:51]
	v_mul_f32_e32 v50, v179, v179
	v_mul_f32_e32 v52, v181, v181
	v_mul_f32_e32 v56, v66, v66
	v_mul_f32_e32 v57, v67, v67
	v_pk_fma_f32 v[50:51], v[178:179], v[178:179], v[50:51] op_sel_hi:[1,1,0]
	v_pk_fma_f32 v[52:53], v[180:181], v[180:181], v[52:53] op_sel_hi:[1,1,0]
	v_mov_b32_e32 v51, v56
	v_mov_b32_e32 v53, v57
	v_pk_add_f32 v[50:51], v[50:51], v[52:53]
	s_mov_b32 s20, s0
	v_pk_add_f32 v[48:49], v[48:49], v[50:51]
	s_add_i32 s0, s0, 8
	v_add_f32_e32 v47, v48, v49
	s_cmp_ge_i32 s0, s3
	s_cselect_b64 s[22:23], -1, 0
	v_add_f32_dpp v47, v47, v47 quad_perm:[1,0,3,2] row_mask:0xf bank_mask:0xf bound_ctrl:1
	s_cmp_lt_i32 s0, s3
	s_cselect_b32 s20, s0, s20
	v_add_f32_dpp v47, v47, v47 quad_perm:[2,3,0,1] row_mask:0xf bank_mask:0xf bound_ctrl:1
	ds_swizzle_b32 v48, v47 offset:swizzle(SWAP,4)
	s_ashr_i32 s21, s20, 31
	s_lshl_b64 s[20:21], s[20:21], 12
	v_lshl_add_u64 v[56:57], v[32:33], 0, s[20:21]
	s_mov_b32 s20, 0xf800000
	s_waitcnt lgkmcnt(0)
	v_add_f32_e32 v47, v47, v48
	ds_swizzle_b32 v48, v47 offset:swizzle(SWAP,8)
	s_waitcnt lgkmcnt(0)
	v_add_f32_e32 v47, v47, v48
	v_mov_b32_e32 v48, v47
	s_waitcnt lgkmcnt(0)
	s_nop 1
	v_permlane16_swap_b32_e32 v47, v48
	v_add_f32_e32 v47, v47, v48
	v_mov_b32_e32 v48, v47
	s_waitcnt lgkmcnt(0)
	s_nop 1
	v_permlane32_swap_b32_e32 v47, v48
	v_add_f32_e32 v47, v47, v48
	v_fmamk_f32 v47, v47, 0x3a000000, v164
	v_mul_f32_e32 v48, 0x4f800000, v47
	v_cmp_gt_f32_e32 vcc, s20, v47
	s_nop 1
	v_cndmask_b32_e32 v47, v47, v48, vcc
	v_sqrt_f32_e32 v58, v47
	global_load_dwordx2 v[50:51], v[56:57], off
	global_load_dwordx2 v[52:53], v[56:57], off offset:512
	global_load_dwordx2 v[54:55], v[56:57], off offset:1024
	global_load_dwordx2 v[48:49], v[56:57], off offset:1536
	v_add_u32_e32 v59, -1, v58
	v_fma_f32 v60, -v59, v58, v47
	v_cmp_ge_f32_e64 s[20:21], 0, v60
	v_add_u32_e32 v60, 1, v58
	s_nop 0
	v_cndmask_b32_e64 v59, v58, v59, s[20:21]
	v_fma_f32 v58, -v60, v58, v47
	v_cmp_lt_f32_e64 s[20:21], 0, v58
	s_nop 1
	v_cndmask_b32_e64 v58, v59, v60, s[20:21]
	v_mul_f32_e32 v59, 0x37800000, v58
	v_cndmask_b32_e32 v58, v58, v59, vcc
	v_cmp_class_f32_e32 vcc, v47, v165
	s_nop 1
	v_cndmask_b32_e32 v47, v58, v47, vcc
	v_div_scale_f32 v64, s[20:21], v47, v47, 1.0
	v_rcp_f32_e32 v68, v64
	s_mov_b32 s20, 0x3d600000
	global_load_dwordx2 v[58:59], v[56:57], off offset:2048
	global_load_dwordx2 v[60:61], v[56:57], off offset:2560
	global_load_dwordx2 v[62:63], v[56:57], off offset:3072
	s_nop 0
	global_load_dwordx2 v[56:57], v[56:57], off offset:3584
	v_fma_f32 v70, -v64, v68, 1.0
	v_fmac_f32_e32 v68, v70, v68
	v_div_scale_f32 v70, vcc, 1.0, v47, 1.0
	v_mul_f32_e32 v86, v70, v68
	v_fma_f32 v87, -v64, v86, v70
	v_fmac_f32_e32 v86, v87, v68
	v_fma_f32 v64, -v64, v86, v70
	v_div_fmas_f32 v64, v64, v68, v86
; #define LAS __attribute__((address_space(3)))
; DI unsigned pk2(float lo, float hi) { const f32x2 v = {lo, hi}; return __builtin_bit_cast(unsigned, __builtin_convertvector(v, bf16x2_t)); }
; DI unsigned pk4_fp8(float a, float b, float c, float d) { unsigned w = 0u; w = __builtin_amdgcn_cvt_pk_fp8_f32(a, b, w, false); w = __builtin_amdgcn_cvt_pk_fp8_f32(c, d, w, true); return w; }
; DI float wave_sum(float v) { v += shx<1>(v); v += shx<2>(v); v += shx<4>(v); v += shx<8>(v); v += shx<16>(v); v += shx<32>(v); return v; }
; template <int MODE, bool SB  > DI void norm_phase(const Params& P, const Frame& F, int L, const void* src_, const float* gain, bool combine) {
;     ...
;         const float rstd = 1.0f / sqrtf(wave_sum(ss) * (1.0f / D) + EPS);
; #pragma unroll
;         for (int j = 0; j < 8; ++j) v[j] = v[j] * rstd * g[j];
;         if (MODE == 4) {
; #pragma unroll
;             for (int j = 0; j < 8; ++j) *(f32x4*)(P.out + (size_t)row * D + 4 * F.lane + 256 * j) = v[j];
;         } else if (MODE == 0 || MODE == 2 || (MODE == 3 && L == 1)) {
;             unsigned* o4 = (unsigned*)((unsigned char*)HN + (size_t)row * D) + F.lane; const float hs = (float)(1 << LS_HN);
; #pragma unroll
;             for (int j = 0; j < 8; ++j) o4[64 * j] = pk4_fp8(v[j][0] * hs, v[j][1] * hs, v[j][2] * hs, v[j][3] * hs);
;         } else {
;             unsigned long long* o8 = (unsigned long long*)(HN + (size_t)row * D) + F.lane;
; #pragma unroll
;             for (int j = 0; j < 8; ++j) o8[64 * j] = (unsigned long long)pk2(v[j][0], v[j][1]) | ((unsigned long long)pk2(v[j][2], v[j][3]) << 32);
;         }
;         if (MODE == 1) {
;             float s[16];
; #pragma unroll
;             for (int q = 0; q < 16; ++q) { float t = 0.f;
; #pragma unroll
;                 for (int j = 0; j < 8; ++j) { const f32x4 w = *(const LAS f32x4*)(F.lds + (size_t)(q * D + 256 * j + 4 * F.lane) * 4); t += (v[j][0] * w[0] + v[j][1] * w[1]) + (v[j][2] * w[2] + v[j][3] * w[3]); }
;                 s[q] = t; if ((q & 3) == 3) asm volatile("" ::: "memory"); }
	v_div_fixup_f32 v96, v64, v47, 1.0
	v_pk_mul_f32 v[74:75], v[96:97], v[74:75] op_sel_hi:[0,1]
	v_mov_b32_e32 v68, v65
	v_pk_mul_f32 v[76:77], v[96:97], v[76:77] op_sel_hi:[0,1]
	v_pk_mul_f32 v[92:93], v[8:9], v[74:75]
	v_mov_b32_e32 v75, v80
	v_mov_b32_e32 v80, v79
	v_pk_mul_f32 v[64:65], v[68:69], v[96:97] op_sel_hi:[1,0]
	v_pk_mul_f32 v[90:91], v[10:11], v[76:77]
	v_mov_b32_e32 v74, v78
	v_pk_mul_f32 v[76:77], v[96:97], v[80:81] op_sel_hi:[0,1]
	v_pk_mul_f32 v[86:87], v[12:13], v[64:65]
	v_mov_b32_e32 v64, v170
	v_mov_b32_e32 v65, v172
	v_pk_mul_f32 v[74:75], v[96:97], v[74:75] op_sel_hi:[0,1]
	v_pk_mul_f32 v[88:89], v[2:3], v[76:77]
	v_pk_mul_f32 v[76:77], v[96:97], v[84:85] op_sel_hi:[0,1]
	v_pk_mul_f32 v[68:69], v[72:73], v[96:97] op_sel_hi:[1,0]
	v_pk_mul_f32 v[64:65], v[96:97], v[64:65] op_sel_hi:[0,1]
	v_mov_b32_e32 v172, v171
	v_pk_mul_f32 v[94:95], v[0:1], v[74:75]
	v_pk_mul_f32 v[74:75], v[96:97], v[82:83] op_sel_hi:[0,1]
	v_pk_mul_f32 v[82:83], v[6:7], v[76:77]
	v_pk_mul_f32 v[78:79], v[14:15], v[68:69]
	v_pk_mul_f32 v[68:69], v[96:97], v[172:173] op_sel_hi:[0,1]
	v_pk_mul_f32 v[76:77], v[16:17], v[64:65]
	v_mov_b32_e32 v64, v174
	v_mov_b32_e32 v65, v176
	v_mov_b32_e32 v176, v175
	v_pk_mul_f32 v[84:85], v[4:5], v[74:75]
	v_pk_mul_f32 v[74:75], v[18:19], v[68:69]
	v_pk_mul_f32 v[64:65], v[96:97], v[64:65] op_sel_hi:[0,1]
	v_pk_mul_f32 v[68:69], v[96:97], v[176:177] op_sel_hi:[0,1]
	v_mov_b32_e32 v70, v97
	v_pk_mul_f32 v[72:73], v[22:23], v[68:69]
	v_pk_mul_f32 v[80:81], v[20:21], v[64:65]
	v_pk_mul_f32 v[68:69], v[96:97], v[178:179] op_sel_hi:[0,1]
	v_pk_mul_f32 v[64:65], v[96:97], v[180:181] op_sel_hi:[0,1]
	v_pk_mul_f32 v[70:71], v[70:71], v[96:97] op_sel_hi:[1,0]
	v_pk_mul_f32 v[66:67], v[66:67], v[96:97] op_sel_hi:[1,0]
	v_lshl_add_u64 v[96:97], s[54:55], 0, v[44:45]
	v_add_co_u32_e32 v96, vcc, s20, v96
	v_cvt_pk_bf16_f32 v170, v92, v93
	v_cvt_pk_bf16_f32 v171, v90, v91
	v_addc_co_u32_e32 v97, vcc, 0, v97, vcc
	global_store_dwordx2 v[96:97], v[170:171], off
	v_cvt_pk_bf16_f32 v170, v94, v95
	v_cvt_pk_bf16_f32 v171, v88, v89
	global_store_dwordx2 v[96:97], v[170:171], off offset:512
	v_cvt_pk_bf16_f32 v170, v84, v85
	v_cvt_pk_bf16_f32 v171, v82, v83
	global_store_dwordx2 v[96:97], v[170:171], off offset:1024
	v_cvt_pk_bf16_f32 v170, v86, v87
	v_cvt_pk_bf16_f32 v171, v78, v79
	global_store_dwordx2 v[96:97], v[170:171], off offset:1536
	v_cvt_pk_bf16_f32 v170, v76, v77
	v_cvt_pk_bf16_f32 v171, v74, v75
	v_pk_mul_f32 v[64:65], v[26:27], v[64:65]
	v_pk_mul_f32 v[68:69], v[24:25], v[68:69]
	global_store_dwordx2 v[96:97], v[170:171], off offset:2048
	v_cvt_pk_bf16_f32 v170, v80, v81
	v_cvt_pk_bf16_f32 v171, v72, v73
	global_store_dwordx2 v[96:97], v[170:171], off offset:2560
	v_cvt_pk_bf16_f32 v170, v68, v69
	v_cvt_pk_bf16_f32 v171, v64, v65
	global_store_dwordx2 v[96:97], v[170:171], off offset:3072
	ds_read_b128 v[196:199], v99
	ds_read_b128 v[200:203], v99 offset:1024
	ds_read_b128 v[204:207], v99 offset:2048
	ds_read_b128 v[208:211], v99 offset:3072
	ds_read_b128 v[212:215], v99 offset:4096
	ds_read_b128 v[216:219], v99 offset:5120
	ds_read_b128 v[220:223], v99 offset:6144
	ds_read_b128 v[224:227], v99 offset:7168
	v_pk_mul_f32 v[66:67], v[30:31], v[66:67]
	v_pk_mul_f32 v[70:71], v[28:29], v[70:71]
	v_cvt_pk_bf16_f32 v175, v66, v67
	v_cvt_pk_bf16_f32 v174, v70, v71
	global_store_dwordx2 v[96:97], v[174:175], off offset:3584
	s_waitcnt lgkmcnt(7)
	v_mul_f32_e32 v47, v197, v93
	v_mul_f32_e32 v96, v199, v91
	v_fmac_f32_e32 v47, v196, v92
	v_fmac_f32_e32 v96, v198, v90
	ds_read_b128 v[196:199], v99 offset:8192
	v_add_f32_e32 v47, v47, v96
	s_waitcnt lgkmcnt(7)
	v_mul_f32_e32 v96, v95, v201
	v_mul_f32_e32 v97, v89, v203
	v_fmac_f32_e32 v96, v94, v200
	v_fmac_f32_e32 v97, v88, v202
	ds_read_b128 v[200:203], v99 offset:9216
	v_add_f32_e32 v47, 0, v47
	v_add_f32_e32 v96, v96, v97
	v_add_f32_e32 v47, v96, v47
	s_waitcnt lgkmcnt(7)
	v_mul_f32_e32 v96, v85, v205
	v_mul_f32_e32 v97, v83, v207
	v_fmac_f32_e32 v96, v84, v204
	v_fmac_f32_e32 v97, v82, v206
	ds_read_b128 v[204:207], v99 offset:10240
	v_add_f32_e32 v96, v96, v97
	v_add_f32_e32 v47, v96, v47
	s_waitcnt lgkmcnt(7)
	v_mul_f32_e32 v96, v87, v209
	v_mul_f32_e32 v97, v79, v211
	v_fmac_f32_e32 v96, v86, v208
	v_fmac_f32_e32 v97, v78, v210
	ds_read_b128 v[208:211], v99 offset:11264
	v_add_f32_e32 v96, v96, v97
	v_add_f32_e32 v47, v96, v47
	s_waitcnt lgkmcnt(7)
	v_mul_f32_e32 v96, v77, v213
	v_mul_f32_e32 v97, v75, v215
	v_fmac_f32_e32 v96, v76, v212
	v_fmac_f32_e32 v97, v74, v214
	ds_read_b128 v[212:215], v99 offset:12288
	v_add_f32_e32 v96, v96, v97
	v_add_f32_e32 v47, v96, v47
	s_waitcnt lgkmcnt(7)
	v_mul_f32_e32 v96, v81, v217
	v_mul_f32_e32 v97, v73, v219
	v_fmac_f32_e32 v96, v80, v216
	v_fmac_f32_e32 v97, v72, v218
	ds_read_b128 v[216:219], v99 offset:13312
	v_add_f32_e32 v96, v96, v97
	v_add_f32_e32 v47, v96, v47
	s_waitcnt lgkmcnt(7)
	v_mul_f32_e32 v96, v69, v221
	v_mul_f32_e32 v97, v65, v223
	v_fmac_f32_e32 v96, v68, v220
	v_fmac_f32_e32 v97, v64, v222
	ds_read_b128 v[220:223], v99 offset:14336
	v_add_f32_e32 v96, v96, v97
	v_add_f32_e32 v47, v96, v47
	s_waitcnt lgkmcnt(7)
	v_mul_f32_e32 v96, v71, v225
	v_mul_f32_e32 v97, v67, v227
	v_fmac_f32_e32 v96, v70, v224
	v_fmac_f32_e32 v97, v66, v226
	ds_read_b128 v[224:227], v99 offset:15360
	v_add_f32_e32 v96, v96, v97
	v_add_f32_e32 v47, v96, v47
	s_waitcnt lgkmcnt(7)
	v_mul_f32_e32 v96, v93, v197
	v_mul_f32_e32 v97, v91, v199
	v_fmac_f32_e32 v96, v92, v196
	v_fmac_f32_e32 v97, v90, v198
	ds_read_b128 v[196:199], v99 offset:16384
	v_add_f32_e32 v96, v96, v97
	s_waitcnt lgkmcnt(7)
; #define LAS __attribute__((address_space(3)))
; template <int MODE, bool SB  > DI void norm_phase(const Params& P, const Frame& F, int L, const void* src_, const float* gain, bool combine) {
;     ...
;             for (int q = 0; q < 16; ++q) { float t = 0.f;
; #pragma unroll
;                 for (int j = 0; j < 8; ++j) { const f32x4 w = *(const LAS f32x4*)(F.lds + (size_t)(q * D + 256 * j + 4 * F.lane) * 4); t += (v[j][0] * w[0] + v[j][1] * w[1]) + (v[j][2] * w[2] + v[j][3] * w[3]); }
;                 s[q] = t; if ((q & 3) == 3) asm volatile("" ::: "memory"); }
	v_mul_f32_e32 v97, v95, v201
	v_fmac_f32_e32 v97, v94, v200
	v_mul_f32_e32 v174, v89, v203
	v_fmac_f32_e32 v174, v88, v202
	ds_read_b128 v[200:203], v99 offset:17408
	v_add_f32_e32 v96, 0, v96
	v_add_f32_e32 v97, v97, v174
	v_add_f32_e32 v96, v96, v97
	s_waitcnt lgkmcnt(7)
	v_mul_f32_e32 v97, v85, v205
	v_fmac_f32_e32 v97, v84, v204
	v_mul_f32_e32 v170, v83, v207
	v_fmac_f32_e32 v170, v82, v206
	ds_read_b128 v[204:207], v99 offset:18432
	v_add_f32_e32 v97, v97, v170
	v_add_f32_e32 v96, v96, v97
	s_waitcnt lgkmcnt(7)
	v_mul_f32_e32 v97, v87, v209
	v_fmac_f32_e32 v97, v86, v208
	v_mul_f32_e32 v174, v79, v211
	v_fmac_f32_e32 v174, v78, v210
	ds_read_b128 v[208:211], v99 offset:19456
	v_add_f32_e32 v97, v97, v174
	v_add_f32_e32 v96, v96, v97
	s_waitcnt lgkmcnt(7)
	v_mul_f32_e32 v97, v77, v213
	v_fmac_f32_e32 v97, v76, v212
	v_mul_f32_e32 v170, v75, v215
	v_fmac_f32_e32 v170, v74, v214
	ds_read_b128 v[212:215], v99 offset:20480
	v_add_f32_e32 v97, v97, v170
	v_add_f32_e32 v96, v96, v97
	s_waitcnt lgkmcnt(7)
	v_mul_f32_e32 v97, v81, v217
	v_fmac_f32_e32 v97, v80, v216
	v_mul_f32_e32 v174, v73, v219
	v_fmac_f32_e32 v174, v72, v218
	ds_read_b128 v[216:219], v99 offset:21504
	v_add_f32_e32 v97, v97, v174
	v_add_f32_e32 v96, v96, v97
	s_waitcnt lgkmcnt(7)
	v_mul_f32_e32 v97, v69, v221
	v_fmac_f32_e32 v97, v68, v220
	v_mul_f32_e32 v170, v65, v223
	v_fmac_f32_e32 v170, v64, v222
	ds_read_b128 v[220:223], v99 offset:22528
	v_add_f32_e32 v97, v97, v170
	v_add_f32_e32 v96, v96, v97
	s_waitcnt lgkmcnt(7)
	v_mul_f32_e32 v97, v71, v225
	v_fmac_f32_e32 v97, v70, v224
	v_mul_f32_e32 v174, v67, v227
	v_fmac_f32_e32 v174, v66, v226
	ds_read_b128 v[224:227], v99 offset:23552
	v_add_f32_e32 v97, v97, v174
	v_add_f32_e32 v96, v96, v97
	s_waitcnt lgkmcnt(7)
	v_mul_f32_e32 v97, v93, v197
	v_fmac_f32_e32 v97, v92, v196
	v_mul_f32_e32 v170, v91, v199
	v_fmac_f32_e32 v170, v90, v198
	ds_read_b128 v[196:199], v99 offset:24576
	s_waitcnt lgkmcnt(7)
	v_mul_f32_e32 v175, v95, v201
	v_add_f32_e32 v97, v97, v170
	v_fmac_f32_e32 v175, v94, v200
	v_mul_f32_e32 v174, v89, v203
	v_fmac_f32_e32 v174, v88, v202
	ds_read_b128 v[200:203], v99 offset:25600
	v_add_f32_e32 v97, 0, v97
	v_add_f32_e32 v174, v175, v174
	v_add_f32_e32 v97, v97, v174
	s_waitcnt lgkmcnt(7)
	v_mul_f32_e32 v171, v85, v205
	v_fmac_f32_e32 v171, v84, v204
	v_mul_f32_e32 v170, v83, v207
	v_fmac_f32_e32 v170, v82, v206
	ds_read_b128 v[204:207], v99 offset:26624
	v_add_f32_e32 v170, v171, v170
	s_waitcnt lgkmcnt(7)
	v_mul_f32_e32 v175, v87, v209
	v_add_f32_e32 v97, v97, v170
	v_fmac_f32_e32 v175, v86, v208
	v_mul_f32_e32 v174, v79, v211
	v_fmac_f32_e32 v174, v78, v210
	ds_read_b128 v[208:211], v99 offset:27648
	v_add_f32_e32 v174, v175, v174
	v_add_f32_e32 v97, v97, v174
	s_waitcnt lgkmcnt(7)
	v_mul_f32_e32 v171, v77, v213
	v_fmac_f32_e32 v171, v76, v212
	v_mul_f32_e32 v170, v75, v215
	v_fmac_f32_e32 v170, v74, v214
	ds_read_b128 v[212:215], v99 offset:28672
	v_add_f32_e32 v170, v171, v170
	s_waitcnt lgkmcnt(7)
	v_mul_f32_e32 v175, v81, v217
	v_add_f32_e32 v97, v97, v170
	v_fmac_f32_e32 v175, v80, v216
	v_mul_f32_e32 v174, v73, v219
	v_fmac_f32_e32 v174, v72, v218
	ds_read_b128 v[216:219], v99 offset:29696
	v_add_f32_e32 v174, v175, v174
	v_add_f32_e32 v97, v97, v174
	s_waitcnt lgkmcnt(7)
	v_mul_f32_e32 v171, v69, v221
	v_fmac_f32_e32 v171, v68, v220
	v_mul_f32_e32 v170, v65, v223
	v_fmac_f32_e32 v170, v64, v222
	ds_read_b128 v[220:223], v99 offset:30720
	v_add_f32_e32 v170, v171, v170
	s_waitcnt lgkmcnt(7)
	v_mul_f32_e32 v175, v71, v225
	v_add_f32_e32 v97, v97, v170
	v_fmac_f32_e32 v175, v70, v224
	v_mul_f32_e32 v174, v67, v227
	v_fmac_f32_e32 v174, v66, v226
	ds_read_b128 v[224:227], v99 offset:31744
	v_add_f32_e32 v174, v175, v174
	v_add_f32_e32 v97, v97, v174
	s_waitcnt lgkmcnt(7)
	v_mul_f32_e32 v171, v93, v197
	v_fmac_f32_e32 v171, v92, v196
	v_mul_f32_e32 v170, v91, v199
	v_fmac_f32_e32 v170, v90, v198
	ds_read_b128 v[196:199], v99 offset:32768
	v_add_f32_e32 v170, v171, v170
	s_waitcnt lgkmcnt(7)
	v_mul_f32_e32 v175, v95, v201
	v_add_f32_e32 v178, 0, v170
	v_fmac_f32_e32 v175, v94, v200
	v_mul_f32_e32 v174, v89, v203
	v_fmac_f32_e32 v174, v88, v202
	ds_read_b128 v[200:203], v99 offset:33792
	v_add_f32_e32 v174, v175, v174
	v_add_f32_e32 v178, v178, v174
	s_waitcnt lgkmcnt(7)
	v_mul_f32_e32 v171, v85, v205
	v_fmac_f32_e32 v171, v84, v204
	v_mul_f32_e32 v170, v83, v207
	v_fmac_f32_e32 v170, v82, v206
	ds_read_b128 v[204:207], v99 offset:34816
	v_add_f32_e32 v170, v171, v170
	s_waitcnt lgkmcnt(7)
	v_mul_f32_e32 v175, v87, v209
	v_add_f32_e32 v178, v178, v170
	v_fmac_f32_e32 v175, v86, v208
	v_mul_f32_e32 v174, v79, v211
	v_fmac_f32_e32 v174, v78, v210
	ds_read_b128 v[208:211], v99 offset:35840
	v_add_f32_e32 v174, v175, v174
	v_add_f32_e32 v178, v178, v174
	s_waitcnt lgkmcnt(7)
	v_mul_f32_e32 v171, v77, v213
	v_fmac_f32_e32 v171, v76, v212
	v_mul_f32_e32 v170, v75, v215
	v_fmac_f32_e32 v170, v74, v214
	ds_read_b128 v[212:215], v99 offset:36864
	v_add_f32_e32 v170, v171, v170
	s_waitcnt lgkmcnt(7)
	v_mul_f32_e32 v175, v81, v217
	v_add_f32_e32 v178, v178, v170
	v_fmac_f32_e32 v175, v80, v216
	v_mul_f32_e32 v174, v73, v219
	v_fmac_f32_e32 v174, v72, v218
	ds_read_b128 v[216:219], v99 offset:37888
	v_add_f32_e32 v174, v175, v174
	v_add_f32_e32 v178, v178, v174
	s_waitcnt lgkmcnt(7)
	v_mul_f32_e32 v171, v69, v221
	v_fmac_f32_e32 v171, v68, v220
	v_mul_f32_e32 v170, v65, v223
	v_fmac_f32_e32 v170, v64, v222
	ds_read_b128 v[220:223], v99 offset:38912
	v_add_f32_e32 v170, v171, v170
	s_waitcnt lgkmcnt(7)
; #define LAS __attribute__((address_space(3)))
; template <int MODE, bool SB  > DI void norm_phase(const Params& P, const Frame& F, int L, const void* src_, const float* gain, bool combine) {
;     ...
;             for (int q = 0; q < 16; ++q) { float t = 0.f;
; #pragma unroll
;                 for (int j = 0; j < 8; ++j) { const f32x4 w = *(const LAS f32x4*)(F.lds + (size_t)(q * D + 256 * j + 4 * F.lane) * 4); t += (v[j][0] * w[0] + v[j][1] * w[1]) + (v[j][2] * w[2] + v[j][3] * w[3]); }
;                 s[q] = t; if ((q & 3) == 3) asm volatile("" ::: "memory"); }
	v_mul_f32_e32 v171, v71, v225
	v_fmac_f32_e32 v171, v70, v224
	v_mul_f32_e32 v177, v67, v227
	v_fmac_f32_e32 v177, v66, v226
	ds_read_b128 v[224:227], v99 offset:39936
	v_add_f32_e32 v170, v178, v170
	v_add_f32_e32 v171, v171, v177
	v_add_f32_e32 v170, v170, v171
	s_waitcnt lgkmcnt(7)
	v_mul_f32_e32 v171, v93, v197
	v_fmac_f32_e32 v171, v92, v196
	v_mul_f32_e32 v172, v91, v199
	v_fmac_f32_e32 v172, v90, v198
	ds_read_b128 v[196:199], v99 offset:40960
	s_waitcnt lgkmcnt(7)
	v_mul_f32_e32 v177, v95, v201
	v_add_f32_e32 v171, v171, v172
	v_fmac_f32_e32 v177, v94, v200
	v_mul_f32_e32 v176, v89, v203
	v_fmac_f32_e32 v176, v88, v202
	ds_read_b128 v[200:203], v99 offset:41984
	v_add_f32_e32 v171, 0, v171
	v_add_f32_e32 v176, v177, v176
	v_add_f32_e32 v171, v171, v176
	s_waitcnt lgkmcnt(7)
	v_mul_f32_e32 v173, v85, v205
	v_fmac_f32_e32 v173, v84, v204
	v_mul_f32_e32 v172, v83, v207
	v_fmac_f32_e32 v172, v82, v206
	ds_read_b128 v[204:207], v99 offset:43008
	v_add_f32_e32 v172, v173, v172
	s_waitcnt lgkmcnt(7)
	v_mul_f32_e32 v177, v87, v209
	v_add_f32_e32 v171, v171, v172
	v_fmac_f32_e32 v177, v86, v208
	v_mul_f32_e32 v176, v79, v211
	v_fmac_f32_e32 v176, v78, v210
	ds_read_b128 v[208:211], v99 offset:44032
	v_add_f32_e32 v176, v177, v176
	v_add_f32_e32 v171, v171, v176
	s_waitcnt lgkmcnt(7)
	v_mul_f32_e32 v173, v77, v213
	v_fmac_f32_e32 v173, v76, v212
	v_mul_f32_e32 v172, v75, v215
	v_fmac_f32_e32 v172, v74, v214
	ds_read_b128 v[212:215], v99 offset:45056
	v_add_f32_e32 v172, v173, v172
	s_waitcnt lgkmcnt(7)
	v_mul_f32_e32 v177, v81, v217
	v_add_f32_e32 v171, v171, v172
	v_fmac_f32_e32 v177, v80, v216
	v_mul_f32_e32 v176, v73, v219
	v_fmac_f32_e32 v176, v72, v218
	ds_read_b128 v[216:219], v99 offset:46080
	v_add_f32_e32 v176, v177, v176
	v_add_f32_e32 v171, v171, v176
	s_waitcnt lgkmcnt(7)
	v_mul_f32_e32 v173, v69, v221
	v_fmac_f32_e32 v173, v68, v220
	v_mul_f32_e32 v172, v65, v223
	v_fmac_f32_e32 v172, v64, v222
	ds_read_b128 v[220:223], v99 offset:47104
	v_add_f32_e32 v172, v173, v172
	s_waitcnt lgkmcnt(7)
	v_mul_f32_e32 v177, v71, v225
	v_add_f32_e32 v171, v171, v172
	v_fmac_f32_e32 v177, v70, v224
	v_mul_f32_e32 v176, v67, v227
	v_fmac_f32_e32 v176, v66, v226
	ds_read_b128 v[224:227], v99 offset:48128
	v_add_f32_e32 v176, v177, v176
	v_add_f32_e32 v171, v171, v176
	s_waitcnt lgkmcnt(7)
	v_mul_f32_e32 v173, v93, v197
	v_fmac_f32_e32 v173, v92, v196
	v_mul_f32_e32 v172, v91, v199
	v_fmac_f32_e32 v172, v90, v198
	ds_read_b128 v[196:199], v99 offset:49152
	v_add_f32_e32 v172, v173, v172
	s_waitcnt lgkmcnt(7)
	v_mul_f32_e32 v177, v95, v201
	v_add_f32_e32 v180, 0, v172
	v_fmac_f32_e32 v177, v94, v200
	v_mul_f32_e32 v176, v89, v203
	v_fmac_f32_e32 v176, v88, v202
	ds_read_b128 v[200:203], v99 offset:50176
	v_add_f32_e32 v176, v177, v176
	v_add_f32_e32 v180, v180, v176
	s_waitcnt lgkmcnt(7)
	v_mul_f32_e32 v173, v85, v205
	v_fmac_f32_e32 v173, v84, v204
	v_mul_f32_e32 v172, v83, v207
	v_fmac_f32_e32 v172, v82, v206
	ds_read_b128 v[204:207], v99 offset:51200
	v_add_f32_e32 v172, v173, v172
	s_waitcnt lgkmcnt(7)
	v_mul_f32_e32 v177, v87, v209
	v_add_f32_e32 v180, v180, v172
	v_fmac_f32_e32 v177, v86, v208
	v_mul_f32_e32 v176, v79, v211
	v_fmac_f32_e32 v176, v78, v210
	ds_read_b128 v[208:211], v99 offset:52224
	v_add_f32_e32 v176, v177, v176
	v_add_f32_e32 v180, v180, v176
	s_waitcnt lgkmcnt(7)
	v_mul_f32_e32 v173, v77, v213
	v_fmac_f32_e32 v173, v76, v212
	v_mul_f32_e32 v172, v75, v215
	v_fmac_f32_e32 v172, v74, v214
	ds_read_b128 v[212:215], v99 offset:53248
	v_add_f32_e32 v172, v173, v172
	s_waitcnt lgkmcnt(7)
	v_mul_f32_e32 v177, v81, v217
	v_add_f32_e32 v180, v180, v172
	v_fmac_f32_e32 v177, v80, v216
	v_mul_f32_e32 v176, v73, v219
	v_fmac_f32_e32 v176, v72, v218
	ds_read_b128 v[216:219], v99 offset:54272
	v_add_f32_e32 v176, v177, v176
	v_add_f32_e32 v180, v180, v176
	s_waitcnt lgkmcnt(7)
	v_mul_f32_e32 v173, v69, v221
	v_fmac_f32_e32 v173, v68, v220
	v_mul_f32_e32 v172, v65, v223
	v_fmac_f32_e32 v172, v64, v222
	ds_read_b128 v[220:223], v99 offset:55296
	v_add_f32_e32 v172, v173, v172
	s_waitcnt lgkmcnt(7)
	v_mul_f32_e32 v173, v71, v225
	v_fmac_f32_e32 v173, v70, v224
	v_mul_f32_e32 v179, v67, v227
	v_fmac_f32_e32 v179, v66, v226
	ds_read_b128 v[224:227], v99 offset:56320
	v_add_f32_e32 v172, v180, v172
	v_add_f32_e32 v173, v173, v179
	v_add_f32_e32 v172, v172, v173
	s_waitcnt lgkmcnt(7)
	v_mul_f32_e32 v173, v93, v197
	v_fmac_f32_e32 v173, v92, v196
	v_mul_f32_e32 v174, v91, v199
	v_fmac_f32_e32 v174, v90, v198
	ds_read_b128 v[196:199], v99 offset:57344
	s_waitcnt lgkmcnt(7)
	v_mul_f32_e32 v179, v95, v201
	v_add_f32_e32 v173, v173, v174
	v_fmac_f32_e32 v179, v94, v200
	v_mul_f32_e32 v178, v89, v203
	v_fmac_f32_e32 v178, v88, v202
	ds_read_b128 v[200:203], v99 offset:58368
	v_add_f32_e32 v173, 0, v173
	v_add_f32_e32 v178, v179, v178
	v_add_f32_e32 v173, v173, v178
	s_waitcnt lgkmcnt(7)
	v_mul_f32_e32 v175, v85, v205
	v_fmac_f32_e32 v175, v84, v204
	v_mul_f32_e32 v174, v83, v207
	v_fmac_f32_e32 v174, v82, v206
	ds_read_b128 v[204:207], v99 offset:59392
	v_add_f32_e32 v174, v175, v174
	s_waitcnt lgkmcnt(7)
	v_mul_f32_e32 v179, v87, v209
	v_add_f32_e32 v173, v173, v174
	v_fmac_f32_e32 v179, v86, v208
	v_mul_f32_e32 v178, v79, v211
	v_fmac_f32_e32 v178, v78, v210
	ds_read_b128 v[208:211], v99 offset:60416
	v_add_f32_e32 v178, v179, v178
	v_add_f32_e32 v173, v173, v178
	s_waitcnt lgkmcnt(7)
	v_mul_f32_e32 v175, v77, v213
	v_fmac_f32_e32 v175, v76, v212
	v_mul_f32_e32 v174, v75, v215
	v_fmac_f32_e32 v174, v74, v214
	ds_read_b128 v[212:215], v99 offset:61440
	v_add_f32_e32 v174, v175, v174
	s_waitcnt lgkmcnt(7)
; #define LAS __attribute__((address_space(3)))
; template <int MODE, bool SB  > DI void norm_phase(const Params& P, const Frame& F, int L, const void* src_, const float* gain, bool combine) {
;     ...
;             for (int q = 0; q < 16; ++q) { float t = 0.f;
; #pragma unroll
;                 for (int j = 0; j < 8; ++j) { const f32x4 w = *(const LAS f32x4*)(F.lds + (size_t)(q * D + 256 * j + 4 * F.lane) * 4); t += (v[j][0] * w[0] + v[j][1] * w[1]) + (v[j][2] * w[2] + v[j][3] * w[3]); }
;                 s[q] = t; if ((q & 3) == 3) asm volatile("" ::: "memory"); }
	v_mul_f32_e32 v179, v81, v217
	v_add_f32_e32 v173, v173, v174
	v_fmac_f32_e32 v179, v80, v216
	v_mul_f32_e32 v178, v73, v219
	v_fmac_f32_e32 v178, v72, v218
	ds_read_b128 v[216:219], v99 offset:62464
	v_add_f32_e32 v178, v179, v178
	v_add_f32_e32 v173, v173, v178
	s_waitcnt lgkmcnt(7)
	v_mul_f32_e32 v175, v69, v221
	v_fmac_f32_e32 v175, v68, v220
	v_mul_f32_e32 v174, v65, v223
	v_fmac_f32_e32 v174, v64, v222
	ds_read_b128 v[220:223], v99 offset:63488
	v_add_f32_e32 v174, v175, v174
	s_waitcnt lgkmcnt(7)
	v_mul_f32_e32 v179, v71, v225
	v_add_f32_e32 v173, v173, v174
	v_fmac_f32_e32 v179, v70, v224
	v_mul_f32_e32 v178, v67, v227
	v_fmac_f32_e32 v178, v66, v226
	ds_read_b128 v[224:227], v99 offset:64512
	v_add_f32_e32 v178, v179, v178
	v_add_f32_e32 v173, v173, v178
	s_waitcnt lgkmcnt(7)
	v_mul_f32_e32 v175, v93, v197
	v_fmac_f32_e32 v175, v92, v196
	v_mul_f32_e32 v174, v91, v199
	v_fmac_f32_e32 v174, v90, v198
	ds_read_b128 v[196:199], v100
	v_add_f32_e32 v174, v175, v174
	s_waitcnt lgkmcnt(7)
	v_mul_f32_e32 v179, v95, v201
	v_add_f32_e32 v182, 0, v174
	v_fmac_f32_e32 v179, v94, v200
	v_mul_f32_e32 v178, v89, v203
	v_fmac_f32_e32 v178, v88, v202
	ds_read_b128 v[200:203], v101
	v_add_f32_e32 v178, v179, v178
	v_add_f32_e32 v182, v182, v178
	s_waitcnt lgkmcnt(7)
	v_mul_f32_e32 v175, v85, v205
	v_fmac_f32_e32 v175, v84, v204
	v_mul_f32_e32 v174, v83, v207
	v_fmac_f32_e32 v174, v82, v206
	ds_read_b128 v[204:207], v102
	v_add_f32_e32 v174, v175, v174
	s_waitcnt lgkmcnt(7)
	v_mul_f32_e32 v179, v87, v209
	v_add_f32_e32 v182, v182, v174
	v_fmac_f32_e32 v179, v86, v208
	v_mul_f32_e32 v178, v79, v211
	v_fmac_f32_e32 v178, v78, v210
	ds_read_b128 v[208:211], v103
	v_add_f32_e32 v178, v179, v178
	v_add_f32_e32 v182, v182, v178
	s_waitcnt lgkmcnt(7)
	v_mul_f32_e32 v175, v77, v213
	v_fmac_f32_e32 v175, v76, v212
	v_mul_f32_e32 v174, v75, v215
	v_fmac_f32_e32 v174, v74, v214
	ds_read_b128 v[212:215], v104
	v_add_f32_e32 v174, v175, v174
	s_waitcnt lgkmcnt(7)
	v_mul_f32_e32 v179, v81, v217
	v_add_f32_e32 v182, v182, v174
	v_fmac_f32_e32 v179, v80, v216
	v_mul_f32_e32 v178, v73, v219
	v_fmac_f32_e32 v178, v72, v218
	ds_read_b128 v[216:219], v105
	v_add_f32_e32 v178, v179, v178
	v_add_f32_e32 v182, v182, v178
	s_waitcnt lgkmcnt(7)
	v_mul_f32_e32 v175, v69, v221
	v_fmac_f32_e32 v175, v68, v220
	v_mul_f32_e32 v174, v65, v223
	v_fmac_f32_e32 v174, v64, v222
	ds_read_b128 v[220:223], v106
	v_add_f32_e32 v174, v175, v174
	s_waitcnt lgkmcnt(7)
	v_mul_f32_e32 v175, v71, v225
	v_fmac_f32_e32 v175, v70, v224
	v_mul_f32_e32 v181, v67, v227
	v_fmac_f32_e32 v181, v66, v226
	ds_read_b128 v[224:227], v107
	v_add_f32_e32 v174, v182, v174
	v_add_f32_e32 v175, v175, v181
	v_add_f32_e32 v174, v174, v175
	s_waitcnt lgkmcnt(7)
	v_mul_f32_e32 v175, v93, v197
	v_fmac_f32_e32 v175, v92, v196
	v_mul_f32_e32 v176, v91, v199
	v_fmac_f32_e32 v176, v90, v198
	ds_read_b128 v[196:199], v108
	s_waitcnt lgkmcnt(7)
	v_mul_f32_e32 v181, v95, v201
	v_add_f32_e32 v175, v175, v176
	v_fmac_f32_e32 v181, v94, v200
	v_mul_f32_e32 v180, v89, v203
	v_fmac_f32_e32 v180, v88, v202
	ds_read_b128 v[200:203], v109
	v_add_f32_e32 v175, 0, v175
	v_add_f32_e32 v180, v181, v180
	v_add_f32_e32 v175, v175, v180
	s_waitcnt lgkmcnt(7)
	v_mul_f32_e32 v177, v85, v205
	v_fmac_f32_e32 v177, v84, v204
	v_mul_f32_e32 v176, v83, v207
	v_fmac_f32_e32 v176, v82, v206
	ds_read_b128 v[204:207], v110
	v_add_f32_e32 v176, v177, v176
	s_waitcnt lgkmcnt(7)
	v_mul_f32_e32 v181, v87, v209
	v_add_f32_e32 v175, v175, v176
	v_fmac_f32_e32 v181, v86, v208
	v_mul_f32_e32 v180, v79, v211
	v_fmac_f32_e32 v180, v78, v210
	ds_read_b128 v[208:211], v111
	v_add_f32_e32 v180, v181, v180
	v_add_f32_e32 v175, v175, v180
	s_waitcnt lgkmcnt(7)
	v_mul_f32_e32 v177, v77, v213
	v_fmac_f32_e32 v177, v76, v212
	v_mul_f32_e32 v176, v75, v215
	v_fmac_f32_e32 v176, v74, v214
	ds_read_b128 v[212:215], v112
	v_add_f32_e32 v176, v177, v176
	s_waitcnt lgkmcnt(7)
	v_mul_f32_e32 v181, v81, v217
	v_add_f32_e32 v175, v175, v176
	v_fmac_f32_e32 v181, v80, v216
	v_mul_f32_e32 v180, v73, v219
	v_fmac_f32_e32 v180, v72, v218
	ds_read_b128 v[216:219], v113
	v_add_f32_e32 v180, v181, v180
	v_add_f32_e32 v175, v175, v180
	s_waitcnt lgkmcnt(7)
	v_mul_f32_e32 v177, v69, v221
	v_fmac_f32_e32 v177, v68, v220
	v_mul_f32_e32 v176, v65, v223
	v_fmac_f32_e32 v176, v64, v222
	ds_read_b128 v[220:223], v114
	v_add_f32_e32 v176, v177, v176
	s_waitcnt lgkmcnt(7)
	v_mul_f32_e32 v181, v71, v225
	v_add_f32_e32 v175, v175, v176
	v_fmac_f32_e32 v181, v70, v224
	v_mul_f32_e32 v180, v67, v227
	v_fmac_f32_e32 v180, v66, v226
	ds_read_b128 v[224:227], v115
	v_add_f32_e32 v180, v181, v180
	v_add_f32_e32 v175, v175, v180
	s_waitcnt lgkmcnt(7)
	v_mul_f32_e32 v177, v93, v197
	v_fmac_f32_e32 v177, v92, v196
	v_mul_f32_e32 v176, v91, v199
	v_fmac_f32_e32 v176, v90, v198
	ds_read_b128 v[196:199], v116
	v_add_f32_e32 v176, v177, v176
	s_waitcnt lgkmcnt(7)
	v_mul_f32_e32 v181, v95, v201
	v_add_f32_e32 v184, 0, v176
	v_fmac_f32_e32 v181, v94, v200
	v_mul_f32_e32 v180, v89, v203
	v_fmac_f32_e32 v180, v88, v202
	ds_read_b128 v[200:203], v117
	v_add_f32_e32 v180, v181, v180
	v_add_f32_e32 v184, v184, v180
	s_waitcnt lgkmcnt(7)
	v_mul_f32_e32 v177, v85, v205
	v_fmac_f32_e32 v177, v84, v204
	v_mul_f32_e32 v176, v83, v207
	v_fmac_f32_e32 v176, v82, v206
	ds_read_b128 v[204:207], v118
	v_add_f32_e32 v176, v177, v176
	s_waitcnt lgkmcnt(7)
	v_mul_f32_e32 v181, v87, v209
	v_add_f32_e32 v184, v184, v176
	v_fmac_f32_e32 v181, v86, v208
	v_mul_f32_e32 v180, v79, v211
	v_fmac_f32_e32 v180, v78, v210
	ds_read_b128 v[208:211], v119
	v_add_f32_e32 v180, v181, v180
	v_add_f32_e32 v184, v184, v180
	s_waitcnt lgkmcnt(7)
; #define LAS __attribute__((address_space(3)))
; template <int MODE, bool SB  > DI void norm_phase(const Params& P, const Frame& F, int L, const void* src_, const float* gain, bool combine) {
;     ...
;             for (int q = 0; q < 16; ++q) { float t = 0.f;
; #pragma unroll
;                 for (int j = 0; j < 8; ++j) { const f32x4 w = *(const LAS f32x4*)(F.lds + (size_t)(q * D + 256 * j + 4 * F.lane) * 4); t += (v[j][0] * w[0] + v[j][1] * w[1]) + (v[j][2] * w[2] + v[j][3] * w[3]); }
;                 s[q] = t; if ((q & 3) == 3) asm volatile("" ::: "memory"); }
	v_mul_f32_e32 v177, v77, v213
	v_fmac_f32_e32 v177, v76, v212
	v_mul_f32_e32 v176, v75, v215
	v_fmac_f32_e32 v176, v74, v214
	ds_read_b128 v[212:215], v120
	v_add_f32_e32 v176, v177, v176
	s_waitcnt lgkmcnt(7)
	v_mul_f32_e32 v181, v81, v217
	v_add_f32_e32 v184, v184, v176
	v_fmac_f32_e32 v181, v80, v216
	v_mul_f32_e32 v180, v73, v219
	v_fmac_f32_e32 v180, v72, v218
	ds_read_b128 v[216:219], v121
	v_add_f32_e32 v180, v181, v180
	v_add_f32_e32 v184, v184, v180
	s_waitcnt lgkmcnt(7)
	v_mul_f32_e32 v177, v69, v221
	v_fmac_f32_e32 v177, v68, v220
	v_mul_f32_e32 v176, v65, v223
	v_fmac_f32_e32 v176, v64, v222
	ds_read_b128 v[220:223], v122
	v_add_f32_e32 v176, v177, v176
	s_waitcnt lgkmcnt(7)
	v_mul_f32_e32 v177, v71, v225
	v_mul_f32_e32 v183, v67, v227
	v_fmac_f32_e32 v177, v70, v224
	v_fmac_f32_e32 v183, v66, v226
	ds_read_b128 v[224:227], v123
	v_add_f32_e32 v176, v184, v176
	v_add_f32_e32 v177, v177, v183
	v_add_f32_e32 v176, v176, v177
	s_waitcnt lgkmcnt(7)
	v_mul_f32_e32 v177, v93, v197
	v_fmac_f32_e32 v177, v92, v196
	v_mul_f32_e32 v178, v91, v199
	s_waitcnt lgkmcnt(6)
	v_mul_f32_e32 v183, v95, v201
	v_fmac_f32_e32 v178, v90, v198
	ds_read_b128 v[196:199], v124
	v_fmac_f32_e32 v183, v94, v200
	v_mul_f32_e32 v182, v89, v203
	v_add_f32_e32 v177, v177, v178
	v_fmac_f32_e32 v182, v88, v202
	ds_read_b128 v[200:203], v125
	v_add_f32_e32 v177, 0, v177
	v_add_f32_e32 v182, v183, v182
	v_add_f32_e32 v177, v177, v182
	s_waitcnt lgkmcnt(7)
	v_mul_f32_e32 v179, v85, v205
	v_fmac_f32_e32 v179, v84, v204
	v_mul_f32_e32 v178, v83, v207
	v_fmac_f32_e32 v178, v82, v206
	ds_read_b128 v[204:207], v126
	s_waitcnt lgkmcnt(7)
	v_mul_f32_e32 v183, v87, v209
	v_add_f32_e32 v178, v179, v178
	v_fmac_f32_e32 v183, v86, v208
	v_mul_f32_e32 v182, v79, v211
	v_add_f32_e32 v177, v177, v178
	v_fmac_f32_e32 v182, v78, v210
	ds_read_b128 v[208:211], v127
	v_add_f32_e32 v182, v183, v182
	v_add_f32_e32 v177, v177, v182
	s_waitcnt lgkmcnt(7)
	v_mul_f32_e32 v179, v77, v213
	v_fmac_f32_e32 v179, v76, v212
	v_mul_f32_e32 v178, v75, v215
	v_fmac_f32_e32 v178, v74, v214
	ds_read_b128 v[212:215], v128
	s_waitcnt lgkmcnt(7)
	v_mul_f32_e32 v183, v81, v217
	v_add_f32_e32 v178, v179, v178
	v_fmac_f32_e32 v183, v80, v216
	v_mul_f32_e32 v182, v73, v219
	v_add_f32_e32 v177, v177, v178
	v_fmac_f32_e32 v182, v72, v218
	ds_read_b128 v[216:219], v129
	v_add_f32_e32 v182, v183, v182
	v_add_f32_e32 v177, v177, v182
	s_waitcnt lgkmcnt(7)
	v_mul_f32_e32 v179, v69, v221
	v_fmac_f32_e32 v179, v68, v220
	v_mul_f32_e32 v178, v65, v223
	v_fmac_f32_e32 v178, v64, v222
	ds_read_b128 v[220:223], v130
	s_waitcnt lgkmcnt(7)
	v_mul_f32_e32 v183, v71, v225
	v_add_f32_e32 v178, v179, v178
	v_fmac_f32_e32 v183, v70, v224
	v_mul_f32_e32 v182, v67, v227
	v_add_f32_e32 v177, v177, v178
	v_fmac_f32_e32 v182, v66, v226
	ds_read_b128 v[224:227], v131
	v_add_f32_e32 v182, v183, v182
	v_add_f32_e32 v177, v177, v182
	s_waitcnt lgkmcnt(7)
	v_mul_f32_e32 v179, v93, v197
	v_fmac_f32_e32 v179, v92, v196
	v_mul_f32_e32 v178, v91, v199
	v_fmac_f32_e32 v178, v90, v198
	ds_read_b128 v[196:199], v132
	s_waitcnt lgkmcnt(7)
	v_mul_f32_e32 v183, v95, v201
	v_add_f32_e32 v178, v179, v178
	v_fmac_f32_e32 v183, v94, v200
	v_mul_f32_e32 v182, v89, v203
	v_add_f32_e32 v186, 0, v178
	v_fmac_f32_e32 v182, v88, v202
	ds_read_b128 v[200:203], v133
	v_add_f32_e32 v182, v183, v182
	v_add_f32_e32 v186, v186, v182
	s_waitcnt lgkmcnt(7)
	v_mul_f32_e32 v179, v85, v205
	v_fmac_f32_e32 v179, v84, v204
	v_mul_f32_e32 v178, v83, v207
	v_fmac_f32_e32 v178, v82, v206
	ds_read_b128 v[204:207], v134
	s_waitcnt lgkmcnt(7)
	v_mul_f32_e32 v183, v87, v209
	v_add_f32_e32 v178, v179, v178
	v_fmac_f32_e32 v183, v86, v208
	v_mul_f32_e32 v182, v79, v211
	v_add_f32_e32 v186, v186, v178
	v_fmac_f32_e32 v182, v78, v210
	ds_read_b128 v[208:211], v135
	v_add_f32_e32 v182, v183, v182
	v_add_f32_e32 v186, v186, v182
	s_waitcnt lgkmcnt(7)
	v_mul_f32_e32 v179, v77, v213
	v_fmac_f32_e32 v179, v76, v212
	v_mul_f32_e32 v178, v75, v215
	v_fmac_f32_e32 v178, v74, v214
	ds_read_b128 v[212:215], v136
	s_waitcnt lgkmcnt(7)
	v_mul_f32_e32 v183, v81, v217
	v_add_f32_e32 v178, v179, v178
	v_fmac_f32_e32 v183, v80, v216
	v_mul_f32_e32 v182, v73, v219
	v_add_f32_e32 v186, v186, v178
	v_fmac_f32_e32 v182, v72, v218
	ds_read_b128 v[216:219], v137
	v_add_f32_e32 v182, v183, v182
	v_add_f32_e32 v186, v186, v182
	s_waitcnt lgkmcnt(7)
	v_mul_f32_e32 v179, v69, v221
	v_fmac_f32_e32 v179, v68, v220
	v_mul_f32_e32 v178, v65, v223
	v_fmac_f32_e32 v178, v64, v222
	ds_read_b128 v[220:223], v138
	s_waitcnt lgkmcnt(7)
	v_mul_f32_e32 v183, v71, v225
	v_add_f32_e32 v178, v179, v178
	v_fmac_f32_e32 v183, v70, v224
	v_mul_f32_e32 v182, v67, v227
	v_add_f32_e32 v186, v186, v178
	v_fmac_f32_e32 v182, v66, v226
	ds_read_b128 v[224:227], v139
	v_add_f32_e32 v182, v183, v182
	v_add_f32_e32 v186, v186, v182
	s_waitcnt lgkmcnt(7)
	v_mul_f32_e32 v179, v93, v197
	v_fmac_f32_e32 v179, v92, v196
	v_mul_f32_e32 v178, v91, v199
	v_fmac_f32_e32 v178, v90, v198
	ds_read_b128 v[196:199], v140
	s_waitcnt lgkmcnt(7)
	v_mul_f32_e32 v183, v95, v201
	v_add_f32_e32 v178, v179, v178
	v_fmac_f32_e32 v183, v94, v200
	v_mul_f32_e32 v182, v89, v203
	v_add_f32_e32 v187, 0, v178
	v_fmac_f32_e32 v182, v88, v202
	ds_read_b128 v[200:203], v141
	v_add_f32_e32 v182, v183, v182
	v_add_f32_e32 v187, v187, v182
	s_waitcnt lgkmcnt(7)
	v_mul_f32_e32 v179, v85, v205
	v_fmac_f32_e32 v179, v84, v204
	v_mul_f32_e32 v178, v83, v207
	v_fmac_f32_e32 v178, v82, v206
	ds_read_b128 v[204:207], v142
	s_waitcnt lgkmcnt(7)
; #define LAS __attribute__((address_space(3)))
; template <int MODE, bool SB  > DI void norm_phase(const Params& P, const Frame& F, int L, const void* src_, const float* gain, bool combine) {
;     ...
;             for (int q = 0; q < 16; ++q) { float t = 0.f;
; #pragma unroll
;                 for (int j = 0; j < 8; ++j) { const f32x4 w = *(const LAS f32x4*)(F.lds + (size_t)(q * D + 256 * j + 4 * F.lane) * 4); t += (v[j][0] * w[0] + v[j][1] * w[1]) + (v[j][2] * w[2] + v[j][3] * w[3]); }
;                 s[q] = t; if ((q & 3) == 3) asm volatile("" ::: "memory"); }
	v_mul_f32_e32 v183, v87, v209
	v_add_f32_e32 v178, v179, v178
	v_fmac_f32_e32 v183, v86, v208
	v_mul_f32_e32 v182, v79, v211
	v_add_f32_e32 v187, v187, v178
	v_fmac_f32_e32 v182, v78, v210
	ds_read_b128 v[208:211], v143
	v_add_f32_e32 v182, v183, v182
	v_add_f32_e32 v187, v187, v182
	s_waitcnt lgkmcnt(7)
	v_mul_f32_e32 v179, v77, v213
	v_fmac_f32_e32 v179, v76, v212
	v_mul_f32_e32 v178, v75, v215
	v_fmac_f32_e32 v178, v74, v214
	ds_read_b128 v[212:215], v144
	s_waitcnt lgkmcnt(7)
	v_mul_f32_e32 v183, v81, v217
	v_add_f32_e32 v178, v179, v178
	v_fmac_f32_e32 v183, v80, v216
	v_mul_f32_e32 v182, v73, v219
	v_add_f32_e32 v187, v187, v178
	v_fmac_f32_e32 v182, v72, v218
	ds_read_b128 v[216:219], v145
	v_add_f32_e32 v182, v183, v182
	v_add_f32_e32 v187, v187, v182
	s_waitcnt lgkmcnt(7)
	v_mul_f32_e32 v179, v69, v221
	v_fmac_f32_e32 v179, v68, v220
	v_mul_f32_e32 v178, v65, v223
	v_fmac_f32_e32 v178, v64, v222
	ds_read_b128 v[220:223], v146
	s_waitcnt lgkmcnt(7)
	v_mul_f32_e32 v183, v71, v225
	v_add_f32_e32 v178, v179, v178
	v_fmac_f32_e32 v183, v70, v224
	v_mul_f32_e32 v182, v67, v227
	v_add_f32_e32 v187, v187, v178
	v_fmac_f32_e32 v182, v66, v226
	ds_read_b128 v[224:227], v147
	v_add_f32_e32 v182, v183, v182
	v_add_f32_e32 v187, v187, v182
	s_waitcnt lgkmcnt(7)
	v_mul_f32_e32 v179, v93, v197
	v_fmac_f32_e32 v179, v92, v196
	v_mul_f32_e32 v178, v91, v199
	v_fmac_f32_e32 v178, v90, v198
	ds_read_b128 v[196:199], v148
	s_waitcnt lgkmcnt(7)
	v_mul_f32_e32 v183, v95, v201
	v_add_f32_e32 v178, v179, v178
	v_fmac_f32_e32 v183, v94, v200
	v_mul_f32_e32 v182, v89, v203
	v_add_f32_e32 v188, 0, v178
	v_fmac_f32_e32 v182, v88, v202
	ds_read_b128 v[200:203], v149
	v_add_f32_e32 v182, v183, v182
	v_add_f32_e32 v188, v188, v182
	s_waitcnt lgkmcnt(7)
	v_mul_f32_e32 v179, v85, v205
	v_fmac_f32_e32 v179, v84, v204
	v_mul_f32_e32 v178, v83, v207
	v_fmac_f32_e32 v178, v82, v206
	ds_read_b128 v[204:207], v150
	s_waitcnt lgkmcnt(7)
	v_mul_f32_e32 v183, v87, v209
	v_add_f32_e32 v178, v179, v178
	v_fmac_f32_e32 v183, v86, v208
	v_mul_f32_e32 v182, v79, v211
	v_add_f32_e32 v188, v188, v178
	v_fmac_f32_e32 v182, v78, v210
	ds_read_b128 v[208:211], v151
	v_add_f32_e32 v182, v183, v182
	v_add_f32_e32 v188, v188, v182
	s_waitcnt lgkmcnt(7)
	v_mul_f32_e32 v179, v77, v213
	v_fmac_f32_e32 v179, v76, v212
	v_mul_f32_e32 v178, v75, v215
	v_fmac_f32_e32 v178, v74, v214
	ds_read_b128 v[212:215], v152
	s_waitcnt lgkmcnt(7)
	v_mul_f32_e32 v183, v81, v217
	v_add_f32_e32 v178, v179, v178
	v_fmac_f32_e32 v183, v80, v216
	v_mul_f32_e32 v182, v73, v219
	v_add_f32_e32 v188, v188, v178
	v_fmac_f32_e32 v182, v72, v218
	ds_read_b128 v[216:219], v153
	v_add_f32_e32 v182, v183, v182
	v_add_f32_e32 v188, v188, v182
	s_waitcnt lgkmcnt(7)
	v_mul_f32_e32 v179, v69, v221
	v_fmac_f32_e32 v179, v68, v220
	v_mul_f32_e32 v178, v65, v223
	v_fmac_f32_e32 v178, v64, v222
	ds_read_b128 v[220:223], v154
	s_waitcnt lgkmcnt(7)
	v_mul_f32_e32 v183, v71, v225
	v_add_f32_e32 v178, v179, v178
	v_fmac_f32_e32 v183, v70, v224
	v_mul_f32_e32 v182, v67, v227
	v_add_f32_e32 v188, v188, v178
	v_fmac_f32_e32 v182, v66, v226
	ds_read_b128 v[224:227], v155
	v_add_f32_e32 v182, v183, v182
	v_add_f32_e32 v188, v188, v182
	s_waitcnt lgkmcnt(7)
	v_mul_f32_e32 v179, v93, v197
	v_fmac_f32_e32 v179, v92, v196
	v_mul_f32_e32 v178, v91, v199
	v_fmac_f32_e32 v178, v90, v198
	ds_read_b128 v[196:199], v156
	s_waitcnt lgkmcnt(7)
	v_mul_f32_e32 v183, v95, v201
	v_add_f32_e32 v178, v179, v178
	v_fmac_f32_e32 v183, v94, v200
	v_mul_f32_e32 v182, v89, v203
	v_add_f32_e32 v189, 0, v178
	v_fmac_f32_e32 v182, v88, v202
	ds_read_b128 v[200:203], v157
	v_add_f32_e32 v182, v183, v182
	v_add_f32_e32 v189, v189, v182
	s_waitcnt lgkmcnt(7)
	v_mul_f32_e32 v179, v85, v205
	v_fmac_f32_e32 v179, v84, v204
	v_mul_f32_e32 v178, v83, v207
	v_fmac_f32_e32 v178, v82, v206
	ds_read_b128 v[204:207], v158
	s_waitcnt lgkmcnt(7)
	v_mul_f32_e32 v183, v87, v209
	v_add_f32_e32 v178, v179, v178
	v_fmac_f32_e32 v183, v86, v208
	v_mul_f32_e32 v182, v79, v211
	v_add_f32_e32 v189, v189, v178
	v_fmac_f32_e32 v182, v78, v210
	ds_read_b128 v[208:211], v159
	v_add_f32_e32 v182, v183, v182
	v_add_f32_e32 v189, v189, v182
	s_waitcnt lgkmcnt(7)
	v_mul_f32_e32 v179, v77, v213
	v_fmac_f32_e32 v179, v76, v212
	v_mul_f32_e32 v178, v75, v215
	v_fmac_f32_e32 v178, v74, v214
	ds_read_b128 v[212:215], v160
	s_waitcnt lgkmcnt(7)
	v_mul_f32_e32 v183, v81, v217
	v_add_f32_e32 v178, v179, v178
	v_fmac_f32_e32 v183, v80, v216
	v_mul_f32_e32 v182, v73, v219
	v_add_f32_e32 v189, v189, v178
	v_fmac_f32_e32 v182, v72, v218
	ds_read_b128 v[216:219], v161
	v_add_f32_e32 v182, v183, v182
	v_add_f32_e32 v189, v189, v182
	s_waitcnt lgkmcnt(7)
	v_mul_f32_e32 v179, v69, v221
	v_fmac_f32_e32 v179, v68, v220
	v_mul_f32_e32 v178, v65, v223
	v_fmac_f32_e32 v178, v64, v222
	ds_read_b128 v[220:223], v162
	s_waitcnt lgkmcnt(7)
	v_mul_f32_e32 v183, v71, v225
	v_add_f32_e32 v178, v179, v178
	v_fmac_f32_e32 v183, v70, v224
	v_mul_f32_e32 v182, v67, v227
	v_add_f32_e32 v189, v189, v178
	v_fmac_f32_e32 v182, v66, v226
	ds_read_b128 v[224:227], v163
	v_add_f32_e32 v182, v183, v182
	v_add_f32_e32 v189, v189, v182
	s_waitcnt lgkmcnt(7)
; #define LAS __attribute__((address_space(3)))
; DI float sigmoidf_(float x) { return __builtin_amdgcn_rcpf(1.0f + __expf(-x)); }
; DI float softplusf_(float x) { return fmaxf(x, 0.f) + log1pf(__expf(-fabsf(x))); }
; template <int MODE, bool SB  > DI void norm_phase(const Params& P, const Frame& F, int L, const void* src_, const float* gain, bool combine) {
;     ...
;                 for (int j = 0; j < 8; ++j) { const f32x4 w = *(const LAS f32x4*)(F.lds + (size_t)(q * D + 256 * j + 4 * F.lane) * 4); t += (v[j][0] * w[0] + v[j][1] * w[1]) + (v[j][2] * w[2] + v[j][3] * w[3]); }
;                 s[q] = t; if ((q & 3) == 3) asm volatile("" ::: "memory"); }
; #pragma unroll
;             for (int i = 0; i < 8; ++i) { const bool hi = (F.lane & 32) != 0; const float send = hi ? s[i] : s[i + 8], keep = hi ? s[i + 8] : s[i]; s[i] = keep + shx<32>(send); }
; #pragma unroll
;             for (int i = 0; i < 4; ++i) { const bool hi = (F.lane & 16) != 0; const float send = hi ? s[i] : s[i + 4], keep = hi ? s[i + 4] : s[i]; s[i] = keep + shx<16>(send); }
; #pragma unroll
;             for (int i = 0; i < 2; ++i) { const bool hi = (F.lane & 8) != 0; const float send = hi ? s[i] : s[i + 2], keep = hi ? s[i + 2] : s[i]; s[i] = keep + shx<8>(send); }
;             { const bool hi = (F.lane & 4) != 0; const float send = hi ? s[0] : s[1], keep = hi ? s[1] : s[0]; s[0] = keep + shx<4>(send); }
;             float mine = s[0]; mine += shx<2>(mine); mine += shx<1>(mine);
;             if ((F.lane & 3) == 0) { const int gi = ((F.lane >> 5) & 1) * 8 + ((F.lane >> 4) & 1) * 4 + ((F.lane >> 3) & 1) * 2 + ((F.lane >> 2) & 1), h = gi & 3; float r;
;                 if (gi < 4) r = sigmoidf_(mine);
;                 else if (gi < 8) r = -__expf(P.in[I_DN_A_LOG][L * 4 + h]) * softplusf_(mine + P.in[I_DN_DT_BIAS][L * 4 + h]);
;                 else if (gi < 12) r = mine + P.in[I_ML_I_BIAS][L * 4 + h];
;                 else r = -softplusf_(-(mine + P.in[I_ML_F_BIAS][L * 4 + h]));
;                 ((float*)(ws + WS_GD))[(size_t)row * 16 + gi] = r; }
	v_mul_f32_e32 v93, v93, v197
	v_mul_f32_e32 v91, v91, v199
	v_fmac_f32_e32 v93, v92, v196
	v_fmac_f32_e32 v91, v90, v198
	v_add_f32_e32 v90, v93, v91
	s_waitcnt lgkmcnt(6)
	v_mul_f32_e32 v95, v95, v201
	v_mul_f32_e32 v89, v89, v203
	v_add_f32_e32 v178, 0, v90
	v_fmac_f32_e32 v95, v94, v200
	v_fmac_f32_e32 v89, v88, v202
	v_add_f32_e32 v88, v95, v89
	v_add_f32_e32 v88, v178, v88
	s_waitcnt lgkmcnt(5)
	v_mul_f32_e32 v85, v85, v205
	v_mul_f32_e32 v83, v83, v207
	v_fmac_f32_e32 v85, v84, v204
	v_fmac_f32_e32 v83, v82, v206
	v_add_f32_e32 v82, v85, v83
	s_waitcnt lgkmcnt(4)
	v_mul_f32_e32 v87, v87, v209
	v_mul_f32_e32 v79, v79, v211
	v_add_f32_e32 v88, v88, v82
	v_fmac_f32_e32 v87, v86, v208
	v_fmac_f32_e32 v79, v78, v210
	v_add_f32_e32 v78, v87, v79
	v_add_f32_e32 v78, v88, v78
	s_waitcnt lgkmcnt(3)
	v_mul_f32_e32 v77, v77, v213
	v_mul_f32_e32 v75, v75, v215
	v_fmac_f32_e32 v77, v76, v212
	v_fmac_f32_e32 v75, v74, v214
	v_add_f32_e32 v74, v77, v75
	s_waitcnt lgkmcnt(2)
	v_mul_f32_e32 v79, v81, v217
	v_mul_f32_e32 v73, v73, v219
	v_add_f32_e32 v78, v78, v74
	v_fmac_f32_e32 v79, v80, v216
	v_fmac_f32_e32 v73, v72, v218
	v_add_f32_e32 v72, v79, v73
	v_add_f32_e32 v72, v78, v72
	s_waitcnt lgkmcnt(1)
	v_mul_f32_e32 v69, v69, v221
	v_mul_f32_e32 v65, v65, v223
	v_fmac_f32_e32 v69, v68, v220
	v_fmac_f32_e32 v65, v64, v222
	v_add_f32_e32 v64, v69, v65
	s_waitcnt lgkmcnt(0)
	v_mul_f32_e32 v65, v71, v225
	v_mul_f32_e32 v67, v67, v227
	v_fmac_f32_e32 v65, v70, v224
	v_fmac_f32_e32 v67, v66, v226
	v_add_f32_e32 v64, v72, v64
	v_add_f32_e32 v65, v65, v67
	v_add_f32_e32 v64, v64, v65
	v_cndmask_b32_e64 v65, v47, v175, s[4:5]
	ds_bpermute_b32 v65, v98, v65
	v_cndmask_b32_e64 v66, v96, v176, s[4:5]
	ds_bpermute_b32 v66, v98, v66
	v_cndmask_b32_e64 v67, v97, v177, s[4:5]
	ds_bpermute_b32 v67, v98, v67
	v_cndmask_b32_e64 v47, v175, v47, s[4:5]
	s_waitcnt lgkmcnt(2)
	v_add_f32_e32 v47, v47, v65
	v_cndmask_b32_e64 v65, v176, v96, s[4:5]
	s_waitcnt lgkmcnt(1)
	v_add_f32_e32 v65, v65, v66
	v_cndmask_b32_e64 v66, v177, v97, s[4:5]
	s_waitcnt lgkmcnt(0)
	v_add_f32_e32 v66, v66, v67
	v_cndmask_b32_e64 v67, v170, v186, s[4:5]
	ds_bpermute_b32 v67, v98, v67
	v_cndmask_b32_e64 v69, v171, v187, s[4:5]
	ds_bpermute_b32 v69, v98, v69
	v_cndmask_b32_e64 v70, v172, v188, s[4:5]
	ds_bpermute_b32 v70, v98, v70
	v_cndmask_b32_e64 v68, v186, v170, s[4:5]
	s_waitcnt lgkmcnt(2)
	v_add_f32_e32 v67, v68, v67
	v_cndmask_b32_e64 v68, v187, v171, s[4:5]
	s_waitcnt lgkmcnt(1)
	v_add_f32_e32 v68, v68, v69
	v_cndmask_b32_e64 v69, v188, v172, s[4:5]
	s_waitcnt lgkmcnt(0)
	v_add_f32_e32 v69, v69, v70
	v_cndmask_b32_e64 v70, v173, v189, s[4:5]
	v_cndmask_b32_e64 v72, v174, v64, s[4:5]
	ds_bpermute_b32 v70, v98, v70
	ds_bpermute_b32 v72, v98, v72
	v_cndmask_b32_e64 v71, v189, v173, s[4:5]
	v_cndmask_b32_e64 v64, v64, v174, s[4:5]
	v_cndmask_b32_e64 v73, v47, v68, s[8:9]
	s_waitcnt lgkmcnt(1)
	v_add_f32_e32 v70, v71, v70
	s_waitcnt lgkmcnt(0)
	v_add_f32_e32 v64, v64, v72
	v_cndmask_b32_e64 v47, v68, v47, s[8:9]
	v_cndmask_b32_e64 v68, v65, v69, s[8:9]
	v_cndmask_b32_e64 v65, v69, v65, s[8:9]
	v_cndmask_b32_e64 v69, v66, v70, s[8:9]
	v_cndmask_b32_e64 v71, v67, v64, s[8:9]
	ds_swizzle_b32 v73, v73 offset:swizzle(SWAP,16)
	ds_swizzle_b32 v68, v68 offset:swizzle(SWAP,16)
	ds_swizzle_b32 v69, v69 offset:swizzle(SWAP,16)
	ds_swizzle_b32 v71, v71 offset:swizzle(SWAP,16)
	v_cndmask_b32_e64 v66, v70, v66, s[8:9]
	v_cndmask_b32_e64 v64, v64, v67, s[8:9]
	s_waitcnt lgkmcnt(3)
	v_add_f32_e32 v47, v47, v73
	s_waitcnt lgkmcnt(2)
	v_add_f32_e32 v65, v65, v68
	s_waitcnt lgkmcnt(1)
	v_add_f32_e32 v66, v66, v69
	s_waitcnt lgkmcnt(0)
	v_add_f32_e32 v64, v64, v71
	v_cndmask_b32_e64 v67, v47, v66, s[10:11]
	v_cndmask_b32_e64 v68, v65, v64, s[10:11]
	ds_swizzle_b32 v67, v67 offset:swizzle(SWAP,8)
	ds_swizzle_b32 v68, v68 offset:swizzle(SWAP,8)
	v_cndmask_b32_e64 v47, v66, v47, s[10:11]
	v_cndmask_b32_e64 v64, v64, v65, s[10:11]
	s_waitcnt lgkmcnt(1)
	v_add_f32_e32 v47, v47, v67
	s_waitcnt lgkmcnt(0)
	v_add_f32_e32 v64, v64, v68
	v_cndmask_b32_e64 v65, v47, v64, s[12:13]
	ds_swizzle_b32 v65, v65 offset:swizzle(SWAP,4)
	v_cndmask_b32_e64 v47, v64, v47, s[12:13]
	s_waitcnt lgkmcnt(0)
	v_add_f32_e32 v47, v47, v65
	s_nop 1
	v_add_f32_dpp v47, v47, v47 quad_perm:[2,3,0,1] row_mask:0xf bank_mask:0xf bound_ctrl:1
	s_nop 1
	v_mov_b32_dpp v64, v47 quad_perm:[1,0,3,2] row_mask:0xf bank_mask:0xf bound_ctrl:1
	s_and_saveexec_b64 s[20:21], s[14:15]
	s_cbranch_execz .LBB0_1647
	v_add_f32_e32 v47, v47, v64
	s_and_saveexec_b64 s[24:25], s[16:17]
	s_xor_b64 s[24:25], exec, s[24:25]
	s_cbranch_execz .LBB0_1659
	s_and_saveexec_b64 s[26:27], s[6:7]
	s_xor_b64 s[26:27], exec, s[26:27]
	s_cbranch_execz .LBB0_1656
	s_and_saveexec_b64 s[28:29], s[18:19]
	s_xor_b64 s[28:29], exec, s[28:29]
	s_cbranch_execz .LBB0_1653
	v_mov_b32_e32 v64, v190
	v_add_f32_e32 v64, v47, v64
